# attention tile stagger shortened: waves 4-7 sleep 64 cycles instead of 128 after each tile barrier
# baseline (speedup 1.0000x reference)
.LBB0_1652:
	s_or_b64 exec, exec, s[8:9]
	s_barrier
	v_readfirstlane_b32 s101, v0
	s_bitcmp1_b32 s101, 8
	s_cbranch_scc0 .Lmy_stagger_ma
	s_sleep 1

.LBB0_1707:
	s_or_b64 exec, exec, s[34:35]
	s_barrier
	v_readfirstlane_b32 s101, v0
	s_bitcmp1_b32 s101, 8
	s_cbranch_scc0 .Lmy_stagger_dl
	s_sleep 1
